# mLSTM num/den and state-update stages: all LDS reads hoisted ahead of the MFMAs, Q fragments reused from the S^T stage, state-stage B fragments read once, reads of the state stage overlapped with the
# speedup vs baseline: 1.0100x; 1.0047x over previous
; #define LAS __attribute__((address_space(3)))
; __device__ __forceinline__ void mlstm_scan_unit(Frame& F, int unit, LAS unsigned* bcnt, unsigned& btarget) {
;     ...
;         { const int mi = w; f32x4 a1[3], a2[3];
; #pragma unroll
;           for (int n = 0; n < 3; ++n) { a1[n] = (f32x4){0.f, 0.f, 0.f, 0.f}; a2[n] = a1[n]; }
; #pragma unroll
;           for (int ks = 0; ks < 2; ++ks) { const s16x8 A = *(const LAS s16x8*)(Ls + (16 * mi + fr) * 72 + 32 * ks + 8 * fq);
; #pragma unroll
;               for (int n = 0; n < 3; ++n) a1[n] = __builtin_amdgcn_mfma_f32_16x16x32_bf16(A, tr_frag(Lv, VS, 32 * ks + 8 * fq, 16 * n, fr), a1[n], 0, 0, 0); }
; #pragma unroll
;           for (int ks = 0; ks < 4; ++ks) { const s16x8 A = *(const LAS s16x8*)(Lq + (16 * mi + fr) * 136 + 32 * ks + 8 * fq);
; #pragma unroll
;               for (int n = 0; n < 3; ++n) a2[n] = __builtin_amdgcn_mfma_f32_16x16x32_bf16(A, *(const LAS s16x8*)(cTc + (16 * n + fr) * 136 + 32 * ks + 8 * fq), a2[n], 0, 0, 0); }
;           const f32x4 mx4 = *(const LAS f32x4*)(smx + 16 * mi + 4 * fq), b4 = *(const LAS f32x4*)(sb + 16 * mi + 4 * fq);
; #pragma unroll
;           for (int rg_ = 0; rg_ < 4; ++rg_) { const float wi = __expf(mstate - mx4[rg_]); float den = a1[2][rg_] + wi * a2[2][rg_]; den = __shfl(den, lane & 48);
;               const float mt = b4[rg_] + mx4[rg_]; const float inv = __builtin_amdgcn_rcpf(fmaxf(fabsf(den), __expf(-mt))); float* hp = HRAW + (tk0 + 16 * mi + 4 * fq + rg_) * RD + mh * 256 + sl * 32 + fr;
;               hp[0] = (a1[0][rg_] + wi * a2[0][rg_]) * inv; hp[16] = (a1[1][rg_] + wi * a2[1][rg_]) * inv; } }
;         {
; #pragma unroll
;           for (int a = 0; a < 2; ++a) {
; #pragma unroll
;               for (int n = 0; n < 3; ++n) st[a][n] = st[a][n] * dec;
.LBB0_948:
	v_add_f32_e32 v41, v127, v66
	v_sub_f32_e32 v41, v41, v93
	v_mul_f32_e32 v41, 0x3fb8aa3b, v41
	v_exp_f32_e32 v100, v41
	v_add_u32_e32 v41, v110, v109
	s_lshl_b32 s0, s71, 6
	s_bitcmp1_b32 s71, 0
	s_cselect_b32 s58, 0x3300, 0
	v_add_u32_e32 v40, s58, v117
	ds_read_b128 v[180:183], v41
	ds_read_b64_tr_b16 v[188:189], v121
	ds_read_b64_tr_b16 v[190:191], v121 offset:448
	ds_read_b64_tr_b16 v[192:193], v121 offset:32
	ds_read_b64_tr_b16 v[194:195], v121 offset:480
	ds_read_b64_tr_b16 v[196:197], v121 offset:64
	ds_read_b64_tr_b16 v[198:199], v121 offset:512
	ds_read_b128 v[184:187], v41 offset:64
	ds_read_b64_tr_b16 v[200:201], v121 offset:3584
	ds_read_b64_tr_b16 v[202:203], v121 offset:4032
	ds_read_b64_tr_b16 v[204:205], v121 offset:3616
	ds_read_b64_tr_b16 v[206:207], v121 offset:4064
	ds_read_b64_tr_b16 v[208:209], v121 offset:3648
	ds_read_b64_tr_b16 v[210:211], v121 offset:4096
	ds_read_b128 v[212:215], v40
	ds_read_b128 v[228:231], v40 offset:4352
	ds_read_b128 v[216:219], v40 offset:64
	ds_read_b128 v[232:235], v40 offset:4416
	ds_read_b128 v[220:223], v40 offset:128
	ds_read_b128 v[152:155], v40 offset:4480
	ds_read_b128 v[224:227], v40 offset:192
	ds_read_b128 v[156:159], v40 offset:4544
	ds_read_b128 v[140:143], v111
	ds_read_b128 v[144:147], v112
	v_lshl_add_u64 v[148:149], v[98:99], 0, s[0:1]
	v_lshlrev_b64 v[148:149], 12, v[148:149]
	v_lshl_add_u64 v[150:151], v[96:97], 0, v[148:149]
	v_pk_mul_f32 v[56:57], v[56:57], v[100:101] op_sel_hi:[1,0]
	v_pk_mul_f32 v[54:55], v[54:55], v[100:101] op_sel_hi:[1,0]
	v_pk_mul_f32 v[60:61], v[60:61], v[100:101] op_sel_hi:[1,0]
	v_pk_mul_f32 v[58:59], v[58:59], v[100:101] op_sel_hi:[1,0]
	v_mul_f32_e64 v64, v64, v100
	v_mul_f32_e64 v65, v65, v100
	v_pk_mul_f32 v[62:63], v[62:63], v[100:101] op_sel_hi:[1,0]
	v_pk_mul_f32 v[44:45], v[44:45], v[100:101] op_sel_hi:[1,0]
	v_pk_mul_f32 v[42:43], v[42:43], v[100:101] op_sel_hi:[1,0]
	v_pk_mul_f32 v[48:49], v[48:49], v[100:101] op_sel_hi:[1,0]
	v_pk_mul_f32 v[46:47], v[46:47], v[100:101] op_sel_hi:[1,0]
	v_pk_mul_f32 v[52:53], v[52:53], v[100:101] op_sel_hi:[1,0]
	v_pk_mul_f32 v[50:51], v[50:51], v[100:101] op_sel_hi:[1,0]
	s_bitcmp1_b32 s70, 0
	s_cselect_b32 s55, 0x3300, 0
	s_waitcnt lgkmcnt(14)
	v_mfma_f32_16x16x32_bf16 v[66:69], v[180:183], v[188:191], 0
	v_mfma_f32_16x16x32_bf16 v[70:73], v[180:183], v[192:195], 0
	v_mfma_f32_16x16x32_bf16 v[74:77], v[180:183], v[196:199], 0
	v_mfma_f32_16x16x32_bf16 v[66:69], v[184:187], v[200:203], v[66:69]
	s_waitcnt lgkmcnt(12)
	v_mfma_f32_16x16x32_bf16 v[70:73], v[184:187], v[204:207], v[70:73]
	s_waitcnt lgkmcnt(10)
	v_mfma_f32_16x16x32_bf16 v[74:77], v[184:187], v[208:211], v[74:77]
	ds_read_b128 v[180:183], v40 offset:8704
	ds_read_b128 v[184:187], v40 offset:8768
	ds_read_b128 v[188:191], v40 offset:8832
	ds_read_b128 v[192:195], v40 offset:8896
	s_waitcnt lgkmcnt(12)
	v_mfma_f32_16x16x32_bf16 v[132:135], v[164:167], v[212:215], 0
	v_mfma_f32_16x16x32_bf16 v[136:139], v[164:167], v[228:231], 0
	s_waitcnt lgkmcnt(10)
	v_mfma_f32_16x16x32_bf16 v[132:135], v[168:171], v[216:219], v[132:135]
	v_mfma_f32_16x16x32_bf16 v[136:139], v[168:171], v[232:235], v[136:139]
	s_waitcnt lgkmcnt(8)
	v_mfma_f32_16x16x32_bf16 v[132:135], v[172:175], v[220:223], v[132:135]
	v_mfma_f32_16x16x32_bf16 v[136:139], v[172:175], v[152:155], v[136:139]
	s_waitcnt lgkmcnt(6)
	v_mfma_f32_16x16x32_bf16 v[132:135], v[176:179], v[224:227], v[132:135]
	v_mfma_f32_16x16x32_bf16 v[136:139], v[176:179], v[156:159], v[136:139]
	s_waitcnt lgkmcnt(3)
	v_mfma_f32_16x16x32_bf16 v[128:131], v[164:167], v[180:183], 0
	s_waitcnt lgkmcnt(2)
	v_mfma_f32_16x16x32_bf16 v[128:131], v[168:171], v[184:187], v[128:131]
	s_waitcnt lgkmcnt(1)
	v_mfma_f32_16x16x32_bf16 v[128:131], v[172:175], v[188:191], v[128:131]
	s_waitcnt lgkmcnt(0)
	v_mfma_f32_16x16x32_bf16 v[128:131], v[176:179], v[192:195], v[128:131]
	s_nop 2
	v_sub_f32_e32 v41, v127, v140
	v_mul_f32_e32 v41, 0x3fb8aa3b, v41
	v_exp_f32_e32 v41, v41
	s_nop 1
	v_fma_f32 v74, v128, v41, v74
	ds_bpermute_b32 v74, v126, v74
	ds_read_b64_tr_b16 v[196:197], v122 offset:62464
	ds_read_b64_tr_b16 v[198:199], v122 offset:63552
	ds_read_b64_tr_b16 v[212:213], v123
	ds_read_b64_tr_b16 v[214:215], v123 offset:448
	ds_read_b64_tr_b16 v[216:217], v123 offset:32
	v_add_f32_e32 v128, v140, v144
	v_mul_f32_e32 v128, 0xbfb8aa3b, v128
	v_exp_f32_e32 v128, v128
	v_fma_f32 v66, v132, v41, v66
	s_waitcnt lgkmcnt(5)
; #define LAS __attribute__((address_space(3)))
; __device__ __forceinline__ unsigned long long pack4bf(f32x4 v) { return (unsigned long long)pk2(v[0], v[1]) | ((unsigned long long)pk2(v[2], v[3]) << 32); }
; __device__ __forceinline__ void mlstm_scan_unit(Frame& F, int unit, LAS unsigned* bcnt, unsigned& btarget) {
;     ...
;           for (int rg_ = 0; rg_ < 4; ++rg_) { const float wi = __expf(mstate - mx4[rg_]); float den = a1[2][rg_] + wi * a2[2][rg_]; den = __shfl(den, lane & 48);
;               const float mt = b4[rg_] + mx4[rg_]; const float inv = __builtin_amdgcn_rcpf(fmaxf(fabsf(den), __expf(-mt))); float* hp = HRAW + (tk0 + 16 * mi + 4 * fq + rg_) * RD + mh * 256 + sl * 32 + fr;
;               hp[0] = (a1[0][rg_] + wi * a2[0][rg_]) * inv; hp[16] = (a1[1][rg_] + wi * a2[1][rg_]) * inv; } }
;         {
; #pragma unroll
;           for (int a = 0; a < 2; ++a) {
; #pragma unroll
;               for (int n = 0; n < 3; ++n) st[a][n] = st[a][n] * dec;
; #pragma unroll
;               for (int ks = 0; ks < 2; ++ks) { const s16x8 A = tr_frag(Lk, 136, 32 * ks + 8 * fq, 16 * (2 * w + a), fr);
; #pragma unroll
;                   for (int n = 0; n < 3; ++n) st[a][n] = __builtin_amdgcn_mfma_f32_16x16x32_bf16(A, tr_frag(Lvs, VS, 32 * ks + 8 * fq, 16 * n, fr), st[a][n], 0, 0, 0); }
; #pragma unroll
;               for (int n = 0; n < 3; ++n) *(LAS unsigned long long*)(cTn + (16 * n + fr) * 136 + 16 * (2 * w + a) + 4 * fq) = pack4bf(st[a][n]); } }
	v_max_f32_e64 v74, |v74|, |v74|
	v_fma_f32 v41, v136, v41, v70
	v_max_f32_e32 v74, v74, v128
	v_rcp_f32_e32 v74, v74
	v_add_f32_e32 v70, v141, v145
	v_mul_f32_e32 v70, 0xbfb8aa3b, v70
	v_exp_f32_e32 v70, v70
	v_mul_f32_e32 v41, v41, v74
	global_store_dword v[150:151], v41, off offset:64
	v_sub_f32_e32 v41, v127, v141
	v_mul_f32_e32 v41, 0x3fb8aa3b, v41
	v_exp_f32_e32 v41, v41
	v_mul_f32_e32 v66, v66, v74
	global_store_dword v[150:151], v66, off
	v_or_b32_e32 v74, 0x1000, v148
	v_fma_f32 v66, v129, v41, v75
	ds_bpermute_b32 v66, v126, v66
	ds_read_b64_tr_b16 v[218:219], v123 offset:480
	ds_read_b64_tr_b16 v[220:221], v123 offset:64
	ds_read_b64_tr_b16 v[222:223], v123 offset:512
	ds_read_b64_tr_b16 v[204:205], v122 offset:62496
	ds_read_b64_tr_b16 v[206:207], v122 offset:63584
	v_mov_b32_e32 v75, v149
	v_fma_f32 v67, v133, v41, v67
	v_fma_f32 v41, v137, v41, v71
	v_lshl_add_u64 v[74:75], v[96:97], 0, v[74:75]
	s_waitcnt lgkmcnt(5)
	v_max_f32_e64 v66, |v66|, |v66|
	v_max_f32_e32 v66, v66, v70
	v_rcp_f32_e32 v66, v66
	s_nop 0
	v_mul_f32_e32 v41, v41, v66
	global_store_dword v[74:75], v41, off offset:64
	v_sub_f32_e32 v41, v127, v142
	v_mul_f32_e32 v41, 0x3fb8aa3b, v41
	v_exp_f32_e32 v41, v41
	v_mul_f32_e32 v67, v67, v66
	global_store_dword v[74:75], v67, off
	v_add_f32_e32 v67, v142, v146
	v_fma_f32 v66, v130, v41, v76
	ds_bpermute_b32 v66, v126, v66
	ds_read_b64_tr_b16 v[200:201], v124 offset:62464
	ds_read_b64_tr_b16 v[202:203], v124 offset:63552
	ds_read_b64_tr_b16 v[224:225], v123 offset:3584
	ds_read_b64_tr_b16 v[226:227], v123 offset:4032
	ds_read_b64_tr_b16 v[228:229], v123 offset:3616
	v_mul_f32_e32 v67, 0xbfb8aa3b, v67
	v_exp_f32_e32 v67, v67
	v_fma_f32 v68, v134, v41, v68
	v_fma_f32 v41, v138, v41, v72
	s_waitcnt lgkmcnt(5)
	v_max_f32_e64 v66, |v66|, |v66|
	v_max_f32_e32 v66, v66, v67
	v_rcp_f32_e32 v70, v66
	v_or_b32_e32 v66, 0x2000, v148
	v_mov_b32_e32 v67, v149
	v_lshl_add_u64 v[66:67], v[96:97], 0, v[66:67]
	v_mul_f32_e32 v41, v41, v70
	global_store_dword v[66:67], v41, off offset:64
	v_sub_f32_e32 v41, v127, v143
	v_mul_f32_e32 v41, 0x3fb8aa3b, v41
	v_exp_f32_e32 v41, v41
	v_mul_f32_e32 v68, v68, v70
	global_store_dword v[66:67], v68, off
	v_add_f32_e32 v67, v143, v147
	v_fmac_f32_e32 v77, v131, v41
	ds_bpermute_b32 v66, v126, v77
	ds_read_b64_tr_b16 v[230:231], v123 offset:4064
	ds_read_b64_tr_b16 v[232:233], v123 offset:3648
	ds_read_b64_tr_b16 v[234:235], v123 offset:4096
	ds_read_b64_tr_b16 v[208:209], v124 offset:62496
	ds_read_b64_tr_b16 v[210:211], v124 offset:63584
	v_mul_f32_e32 v67, 0xbfb8aa3b, v67
	v_exp_f32_e32 v67, v67
	v_or_b32_e32 v148, 0x3000, v148
	v_fmac_f32_e32 v69, v135, v41
	s_waitcnt lgkmcnt(5)
	v_max_f32_e64 v66, |v66|, |v66|
	v_max_f32_e32 v66, v66, v67
	v_rcp_f32_e32 v68, v66
	v_fmac_f32_e32 v73, v139, v41
	v_lshl_add_u64 v[66:67], v[96:97], 0, v[148:149]
	v_mul_f32_e32 v69, v69, v68
	v_mul_f32_e32 v41, v73, v68
	global_store_dword v[66:67], v69, off
	global_store_dword v[66:67], v41, off offset:64
	v_add_u32_e32 v41, s55, v118
	s_waitcnt lgkmcnt(0)
	v_mfma_f32_16x16x32_bf16 v[54:57], v[196:199], v[212:215], v[54:57]
	v_mfma_f32_16x16x32_bf16 v[58:61], v[196:199], v[216:219], v[58:61]
	v_mfma_f32_16x16x32_bf16 v[62:65], v[196:199], v[220:223], v[62:65]
	v_mfma_f32_16x16x32_bf16 v[42:45], v[204:207], v[212:215], v[42:45]
	v_mfma_f32_16x16x32_bf16 v[46:49], v[204:207], v[216:219], v[46:49]
	v_mfma_f32_16x16x32_bf16 v[50:53], v[204:207], v[220:223], v[50:53]
	v_mfma_f32_16x16x32_bf16 v[54:57], v[200:203], v[224:227], v[54:57]
	v_mfma_f32_16x16x32_bf16 v[58:61], v[200:203], v[228:231], v[58:61]
	v_mfma_f32_16x16x32_bf16 v[62:65], v[200:203], v[232:235], v[62:65]
	v_mfma_f32_16x16x32_bf16 v[42:45], v[208:211], v[224:227], v[42:45]
	v_mfma_f32_16x16x32_bf16 v[46:49], v[208:211], v[228:231], v[46:49]
	v_mfma_f32_16x16x32_bf16 v[50:53], v[208:211], v[232:235], v[50:53]
	s_nop 2
	v_cvt_pk_bf16_f32 v66, v54, v55
	v_cvt_pk_bf16_f32 v67, v56, v57
	ds_write_b64 v41, v[66:67]
	v_cvt_pk_bf16_f32 v68, v58, v59
	v_cvt_pk_bf16_f32 v69, v60, v61
	ds_write_b64 v41, v[68:69] offset:4352
	v_cvt_pk_bf16_f32 v70, v62, v63
	v_cvt_pk_bf16_f32 v71, v64, v65
	ds_write_b64 v41, v[70:71] offset:8704
	v_cvt_pk_bf16_f32 v72, v42, v43
	v_cvt_pk_bf16_f32 v73, v44, v45
	ds_write_b64 v41, v[72:73] offset:32
	v_cvt_pk_bf16_f32 v74, v46, v47
	v_cvt_pk_bf16_f32 v75, v48, v49
	ds_write_b64 v41, v[74:75] offset:4384
	v_cvt_pk_bf16_f32 v76, v50, v51
	v_cvt_pk_bf16_f32 v77, v52, v53
	ds_write_b64 v41, v[76:77] offset:8736
	s_waitcnt lgkmcnt(0)
	s_and_saveexec_b64 s[58:59], s[4:5]
	s_cbranch_execz .LBB0_951
	s_mov_b64 s[60:61], exec
	v_mbcnt_lo_u32_b32 v41, s60, 0
	v_mbcnt_hi_u32_b32 v41, s61, v41
	v_cmp_eq_u32_e32 vcc, 0, v41
	s_and_b64 s[62:63], exec, vcc
	s_mov_b64 exec, s[62:63]
	s_bcnt1_i32_b64 s0, s[60:61]
	v_mov_b32_e32 v41, s67
	v_mov_b32_e32 v66, s0
	ds_add_u32 v41, v66
